# speedup vs baseline: 1.0032x; 1.0016x over previous
.LBB2_31:
	v_exp_f32_e32 v49, v40
	v_add_f32_e32 v40, v80, v81
	v_add_f32_e32 v40, v40, v82
	v_add_f32_e32 v40, v40, v83
	v_add_f32_e32 v40, v40, v84
	v_exp_f32_e32 v62, v41
	v_exp_f32_e32 v63, v42
	v_exp_f32_e32 v64, v43
	v_exp_f32_e32 v65, v44
	v_exp_f32_e32 v66, v45
	v_exp_f32_e32 v67, v46
	v_exp_f32_e32 v68, v47
	v_add_f32_e32 v50, v40, v85
	v_cvt_pk_f16_f32 v40, v80, v81
	v_cvt_pk_f16_f32 v41, v82, v83
	v_cvt_pk_f16_f32 v42, v84, v85
	v_cvt_pk_f16_f32 v43, v86, v87
	ds_read_b64_tr_b16 v[44:45], v187 offset:32768
	ds_read_b64_tr_b16 v[46:47], v187 offset:33280
	v_add_f32_e32 v50, v50, v86
	v_add_f32_e32 v54, v50, v87
	ds_read_b64_tr_b16 v[50:51], v187 offset:33792
	ds_read_b64_tr_b16 v[52:53], v187 offset:34304
	s_waitcnt lgkmcnt(2)
	v_mfma_f32_32x32x16_f16 v[0:15], v[40:43], v[44:47], v[0:15]
	ds_read_b64_tr_b16 v[44:45], v187 offset:36864
	ds_read_b64_tr_b16 v[46:47], v187 offset:37376
	v_add_f32_e32 v54, v54, v88
	v_add_f32_e32 v69, v54, v89
	v_cvt_pk_f16_f32 v54, v88, v89
	v_cvt_pk_f16_f32 v55, v90, v91
	v_cvt_pk_f16_f32 v56, v92, v93
	v_cvt_pk_f16_f32 v57, v94, v95
	s_waitcnt lgkmcnt(0)
	v_mfma_f32_32x32x16_f16 v[16:31], v[40:43], v[44:47], v[16:31]
	v_add_f32_e32 v40, v69, v90
	v_add_f32_e32 v40, v40, v91
	v_add_f32_e32 v40, v40, v92
	v_add_f32_e32 v40, v40, v93
	ds_read_b64_tr_b16 v[58:59], v187 offset:37888
	ds_read_b64_tr_b16 v[60:61], v187 offset:38400
	v_add_f32_e32 v40, v40, v94
	v_add_f32_e32 v40, v40, v95
	v_mfma_f32_32x32x16_f16 v[0:15], v[54:57], v[50:53], v[0:15]
	v_add_f32_e32 v40, v40, v32
	v_add_f32_e32 v50, v40, v33
	v_cvt_pk_f16_f32 v40, v32, v33
	v_cvt_pk_f16_f32 v41, v34, v35
	v_cvt_pk_f16_f32 v42, v36, v37
	v_cvt_pk_f16_f32 v43, v38, v39
	ds_read_b64_tr_b16 v[44:45], v187 offset:34816
	ds_read_b64_tr_b16 v[46:47], v187 offset:35328
	s_waitcnt lgkmcnt(2)
	v_mfma_f32_32x32x16_f16 v[16:31], v[54:57], v[58:61], v[16:31]
	v_add_f32_e32 v32, v50, v34
	v_add_f32_e32 v50, v32, v35
	ds_read_b64_tr_b16 v[32:33], v187 offset:35840
	ds_read_b64_tr_b16 v[34:35], v187 offset:36352
	v_add_f32_e32 v36, v50, v36
	v_add_f32_e32 v36, v36, v37
	v_cvt_pk_f16_f32 v50, v49, v62
	v_cvt_pk_f16_f32 v51, v63, v64
	s_waitcnt lgkmcnt(2)
	v_mfma_f32_32x32x16_f16 v[0:15], v[40:43], v[44:47], v[0:15]
	ds_read_b64_tr_b16 v[44:45], v187 offset:38912
	ds_read_b64_tr_b16 v[46:47], v187 offset:39424
	v_cvt_pk_f16_f32 v52, v65, v66
	v_cvt_pk_f16_f32 v53, v67, v68
	ds_read_b64_tr_b16 v[54:55], v187 offset:39936
	ds_read_b64_tr_b16 v[56:57], v187 offset:40448
	v_add_f32_e32 v36, v36, v38
	v_add_f32_e32 v36, v36, v39
	v_add_f32_e32 v36, v36, v49
	s_waitcnt lgkmcnt(2)
	v_mfma_f32_32x32x16_f16 v[16:31], v[40:43], v[44:47], v[16:31]
	v_add_f32_e32 v36, v36, v62
	v_mfma_f32_32x32x16_f16 v[0:15], v[50:53], v[32:35], v[0:15]
	v_add_f32_e32 v32, v36, v63
	v_add_f32_e32 v32, v32, v64
	v_add_f32_e32 v32, v32, v65
	v_add_f32_e32 v32, v32, v66
	v_add_f32_e32 v32, v32, v67
	v_add_f32_e32 v32, v32, v68
	v_add_f32_e32 v32, v188, v32
	s_waitcnt lgkmcnt(0)
	v_mfma_f32_32x32x16_f16 v[16:31], v[50:53], v[54:57], v[16:31]
	v_mov_b32_e32 v33, v32
	s_nop 1
	v_permlane32_swap_b32_e32 v32, v33
	s_and_saveexec_b64 s[2:3], s[0:1]
	v_add_f32_e32 v32, v32, v33
	ds_write_b32 v186, v32 offset:49280
	s_or_b64 exec, exec, s[2:3]
	s_waitcnt lgkmcnt(0)
	ds_read_b128 v[32:35], v48 offset:49280
	ds_read_b128 v[36:39], v48 offset:49312
	s_lshl_b64 s[0:1], s[10:11], 2
	s_add_u32 s0, s6, s0
	s_addc_u32 s1, s7, s1
	s_waitcnt lgkmcnt(1)
	v_rcp_f32_e32 v40, v32
	v_rcp_f32_e32 v41, v33
	s_lshl_b32 s2, s20, 13
	v_rcp_f32_e32 v42, v34
	v_rcp_f32_e32 v43, v35
	s_waitcnt lgkmcnt(0)
	v_rcp_f32_e32 v44, v36
	ds_read_b128 v[32:35], v48 offset:49344
	v_rcp_f32_e32 v45, v37
	v_rcp_f32_e32 v46, v38
	v_rcp_f32_e32 v47, v39
	ds_read_b128 v[36:39], v48 offset:49376
	s_add_i32 s2, s2, 0
	v_lshlrev_b32_e32 v48, 2, v181
	v_add3_u32 v48, s2, v182, v48
	v_mul_f32_e32 v0, v0, v40
	v_mul_f32_e32 v16, v16, v40
	v_add_u32_e32 v40, 0xc800, v48
	ds_write2_b32 v40, v0, v16 offset1:32
	v_mul_f32_e32 v0, v1, v41
	v_mul_f32_e32 v1, v17, v41
	ds_write2_b32 v40, v0, v1 offset0:64 offset1:96
	v_mul_f32_e32 v0, v2, v42
	v_mul_f32_e32 v1, v18, v42
	ds_write2_b32 v40, v0, v1 offset0:128 offset1:160
	v_mul_f32_e32 v0, v3, v43
	v_mul_f32_e32 v1, v19, v43
	s_waitcnt lgkmcnt(4)
	v_rcp_f32_e32 v32, v32
	ds_write2_b32 v40, v0, v1 offset0:192 offset1:224
	v_mul_f32_e32 v0, v4, v44
	v_mul_f32_e32 v1, v20, v44
	v_add_u32_e32 v2, 0xd000, v48
	v_rcp_f32_e32 v33, v33
	ds_write2_b32 v2, v0, v1 offset1:32
	v_mul_f32_e32 v0, v5, v45
	v_mul_f32_e32 v1, v21, v45
	v_rcp_f32_e32 v34, v34
	ds_write2_b32 v2, v0, v1 offset0:64 offset1:96
	v_mul_f32_e32 v0, v6, v46
	v_mul_f32_e32 v1, v22, v46
	v_rcp_f32_e32 v35, v35
	ds_write2_b32 v2, v0, v1 offset0:128 offset1:160
	v_mul_f32_e32 v0, v7, v47
	v_mul_f32_e32 v1, v23, v47
	s_waitcnt lgkmcnt(7)
	v_rcp_f32_e32 v36, v36
	ds_write2_b32 v2, v0, v1 offset0:192 offset1:224
	v_mul_f32_e32 v0, v8, v32
	v_mul_f32_e32 v1, v24, v32
	v_add_u32_e32 v2, 0xd800, v48
	v_rcp_f32_e32 v37, v37
	ds_write2_b32 v2, v0, v1 offset1:32
	v_mul_f32_e32 v0, v9, v33
	v_mul_f32_e32 v1, v25, v33
	v_rcp_f32_e32 v38, v38
	ds_write2_b32 v2, v0, v1 offset0:64 offset1:96
	v_mul_f32_e32 v0, v10, v34
	v_mul_f32_e32 v1, v26, v34
	v_rcp_f32_e32 v39, v39
	ds_write2_b32 v2, v0, v1 offset0:128 offset1:160
	v_mul_f32_e32 v0, v11, v35
	v_mul_f32_e32 v1, v27, v35
	ds_write2_b32 v2, v0, v1 offset0:192 offset1:224
	v_mul_f32_e32 v0, v12, v36
	v_mul_f32_e32 v1, v28, v36
	v_add_u32_e32 v2, 0xe000, v48
	ds_write2_b32 v2, v0, v1 offset1:32
	v_mul_f32_e32 v0, v13, v37
	v_mul_f32_e32 v1, v29, v37
	ds_write2_b32 v2, v0, v1 offset0:64 offset1:96
	v_mul_f32_e32 v0, v14, v38
	v_mul_f32_e32 v1, v30, v38
	ds_write2_b32 v2, v0, v1 offset0:128 offset1:160
	v_mul_f32_e32 v0, v15, v39
	v_mul_f32_e32 v1, v31, v39
	v_and_b32_e32 v8, 0xf0, v185
	ds_write2_b32 v2, v0, v1 offset0:192 offset1:224
	v_add_u32_e32 v14, s2, v8
	s_waitcnt lgkmcnt(0)
	v_lshl_add_u32 v0, v183, 8, v14
	v_or_b32_e32 v15, 4, v183
	s_lshl_b32 s3, s21, 2
	ds_read_b128 v[0:3], v0 offset:51200
	v_lshl_add_u32 v4, v15, 8, v14
	s_add_u32 s0, s0, s3
	ds_read_b128 v[4:7], v4 offset:51200
	s_addc_u32 s1, s1, 0
	v_mov_b32_e32 v9, 0
	v_lshl_add_u64 v[10:11], s[0:1], 0, v[8:9]
	v_lshlrev_b32_e32 v8, 11, v183
	v_lshl_add_u64 v[12:13], v[10:11], 0, v[8:9]
	v_lshlrev_b32_e32 v8, 11, v15
	s_waitcnt lgkmcnt(1)
	global_store_dwordx4 v[12:13], v[0:3], off sc1 nt
	v_or_b32_e32 v15, 12, v183
	s_nop 0
	v_lshl_add_u64 v[0:1], v[10:11], 0, v[8:9]
	s_waitcnt lgkmcnt(0)
	global_store_dwordx4 v[0:1], v[4:7], off sc1 nt
	s_nop 1
	v_or_b32_e32 v4, 8, v183
	v_lshl_add_u32 v0, v4, 8, v14
	ds_read_b128 v[0:3], v0 offset:51200
	v_lshlrev_b32_e32 v8, 11, v4
	v_lshl_add_u32 v4, v15, 8, v14
	ds_read_b128 v[4:7], v4 offset:51200
	v_lshl_add_u64 v[12:13], v[10:11], 0, v[8:9]
	v_lshlrev_b32_e32 v8, 11, v15
	s_waitcnt lgkmcnt(1)
	global_store_dwordx4 v[12:13], v[0:3], off sc1 nt
	v_or_b32_e32 v15, 20, v183
	s_nop 0
	v_lshl_add_u64 v[0:1], v[10:11], 0, v[8:9]
	s_waitcnt lgkmcnt(0)
	global_store_dwordx4 v[0:1], v[4:7], off sc1 nt
	s_nop 1
	v_or_b32_e32 v4, 16, v183
	v_lshl_add_u32 v0, v4, 8, v14
	ds_read_b128 v[0:3], v0 offset:51200
	v_lshlrev_b32_e32 v8, 11, v4
	v_lshl_add_u32 v4, v15, 8, v14
	ds_read_b128 v[4:7], v4 offset:51200
	v_lshl_add_u64 v[12:13], v[10:11], 0, v[8:9]
	v_lshlrev_b32_e32 v8, 11, v15
	s_waitcnt lgkmcnt(1)
	global_store_dwordx4 v[12:13], v[0:3], off sc1 nt
	v_or_b32_e32 v15, 28, v183
	s_nop 0
	v_lshl_add_u64 v[0:1], v[10:11], 0, v[8:9]
	s_waitcnt lgkmcnt(0)
	global_store_dwordx4 v[0:1], v[4:7], off sc1 nt
	s_nop 1
	v_or_b32_e32 v4, 24, v183
	v_lshl_add_u32 v0, v4, 8, v14
	ds_read_b128 v[0:3], v0 offset:51200
	v_lshlrev_b32_e32 v8, 11, v4
	v_lshl_add_u32 v4, v15, 8, v14
	ds_read_b128 v[4:7], v4 offset:51200
	v_lshl_add_u64 v[12:13], v[10:11], 0, v[8:9]
	v_lshlrev_b32_e32 v8, 11, v15
	s_waitcnt lgkmcnt(1)
	global_store_dwordx4 v[12:13], v[0:3], off sc1 nt
	s_nop 1
	v_lshl_add_u64 v[0:1], v[10:11], 0, v[8:9]
	s_waitcnt lgkmcnt(0)
	global_store_dwordx4 v[0:1], v[4:7], off sc1 nt
	s_endpgm
